# RWKV chain loop: MFMAs write the state registers directly (no per-step copies), state bf16 converts and ring-slot index moved to the loop tail
# baseline (speedup 1.0000x reference)
.LBB0_838:
	v_readlane_b32 s6, v255, 54
	s_bfe_u32 s0, s6, 0x10006
	v_readlane_b32 s1, v254, 5
	s_or_b32 s0, s0, s1
	s_lshl_b32 s35, s54, 12
	s_lshl_b32 s50, s57, 10
	s_lshl_b32 s51, s55, 10
	s_lshl_b32 s54, s56, 10
	v_readlane_b32 s1, v254, 60
	s_add_u32 s1, s16, s1
	s_addc_u32 s36, s17, 0
	s_lshl_b32 s0, s0, 5
	s_add_u32 s0, s1, s0
	v_lshrrev_b32_e32 v9, 1, v1
	s_addc_u32 s1, s36, 0
	v_and_b32_e32 v10, 24, v9
	v_mov_b32_e32 v11, v35
	v_lshl_add_u64 v[10:11], s[0:1], 0, v[10:11]
	s_mov_b64 s[0:1], 0x23388000
	v_lshl_add_u64 v[44:45], v[10:11], 0, s[0:1]
	v_readlane_b32 s0, v255, 52
	s_cmp_lt_i32 s0, 2
	s_cselect_b64 s[36:37], -1, 0
	s_lshl_b32 s56, s0, 9
	s_and_b32 s0, s6, 0xfffffc0
	v_or_b32_e32 v9, s0, v140
	v_mov_b32_e32 v10, 0x3c00
	s_and_b64 s[0:1], s[2:3], exec
	v_lshl_add_u32 v65, v9, 4, v10
	v_mov_b32_e32 v9, v35
	s_cselect_b32 s0, s58, 0
	v_lshlrev_b64 v[46:47], 4, v[8:9]
	v_or_b32_e32 v8, s0, v140
	v_readlane_b32 s0, v254, 51
	s_add_u32 s0, s16, s0
	v_readlane_b32 s1, v254, 52
	s_addc_u32 s1, s17, s1
	v_cndmask_b32_e64 v8, v8, v28, s[4:5]
	v_lshl_add_u64 v[52:53], s[0:1], 0, v[6:7]
	v_readlane_b32 s0, v254, 53
	v_or_b32_e32 v10, 64, v140
	v_ashrrev_i32_e32 v9, 31, v8
	s_add_u32 s42, s16, s0
	v_readlane_b32 s0, v254, 55
	v_lshlrev_b64 v[48:49], s44, v[8:9]
	v_cndmask_b32_e64 v8, v26, v10, s[38:39]
	s_addc_u32 s43, s17, s0
	v_readlane_b32 s0, v254, 54
	v_cndmask_b32_e64 v8, v8, v27, s[2:3]
	s_add_u32 s0, s16, s0
	v_readlane_b32 s1, v254, 56
	v_ashrrev_i32_e32 v9, 31, v8
	v_lshl_add_u64 v[54:55], s[42:43], 0, v[4:5]
	s_addc_u32 s1, s17, s1
	v_mov_b32_e32 v4, v35
	v_mov_b32_e32 v5, v35
	v_lshlrev_b64 v[50:51], s44, v[8:9]
	v_lshl_add_u64 v[56:57], s[0:1], 0, v[2:3]
	s_movk_i32 s0, 0x10ff
	v_mov_b32_e32 v2, v35
	v_mov_b32_e32 v3, v35
	v_mov_b64_e32 v[8:9], v[4:5]
	v_mov_b64_e32 v[12:13], v[4:5]
	v_mov_b64_e32 v[16:17], v[4:5]
	v_and_b32_e32 v63, 15, v1
	s_mov_b32 s55, 5
	v_lshlrev_b32_e32 v64, 3, v140
	s_mov_b32 s57, 0
	v_bitop3_b32 v1, v1, s0, 15 bitop3:0x6c
	s_mov_b64 s[44:45], 0
	v_mov_b64_e32 v[6:7], v[2:3]
	v_mov_b64_e32 v[10:11], v[2:3]
	v_mov_b64_e32 v[14:15], v[2:3]
	s_mov_b32 s100, 0
	v_mov_b32_e32 v102, v35
	v_mov_b32_e32 v103, v35
	v_mov_b32_e32 v104, v35
	v_mov_b32_e32 v105, v35
	v_mov_b32_e32 v106, v35
	v_mov_b32_e32 v107, v35
	v_mov_b32_e32 v108, v35
	v_mov_b32_e32 v109, v35
	s_branch .LBB0_842
.Lmy_ch_tail:
	s_add_i32 s57, s57, 1
	s_add_i32 s55, s55, 1
	s_add_u32 s44, s44, 0x5c00
	s_addc_u32 s45, s45, 0
	v_add_u32_e32 v63, 16, v63
	v_add_u32_e32 v1, -16, v1
	s_add_i32 s100, s100, 0x4400
	s_cmp_eq_u32 s100, 0x1dc00
	s_cselect_b32 s100, 0, s100
	v_cvt_pk_bf16_f32 v102, v2, v3
	v_cvt_pk_bf16_f32 v103, v4, v5
	v_cvt_pk_bf16_f32 v104, v6, v7
	v_cvt_pk_bf16_f32 v105, v8, v9
	v_cvt_pk_bf16_f32 v106, v10, v11
	v_cvt_pk_bf16_f32 v107, v12, v13
	v_cvt_pk_bf16_f32 v108, v14, v15
	v_cvt_pk_bf16_f32 v109, v16, v17
	s_cmp_lg_u32 s44, 0x61c000
	s_cbranch_scc0 .LBB0_875
	s_branch .LBB0_842

.LBB0_850:
	s_mov_b64 s[0:1], -1
	s_and_b64 vcc, exec, s[10:11]
	s_barrier
	s_cbranch_vccz .LBB0_857
	s_andn2_b64 vcc, exec, s[36:37]
	s_cbranch_vccnz .LBB0_866
	s_mov_b32 s0, s100
	s_add_i32 s1, s0, s56
	v_add_u32_e32 v58, s0, v34
	v_add_u32_e32 v59, s1, v64
	ds_read_b128 v[18:21], v58
	ds_read_b128 v[22:25], v58 offset:1024
	ds_read2st64_b64 v[26:29], v59 offset0:22 offset1:24
	ds_read_b128 v[30:33], v58 offset:2048
	ds_read_b128 v[36:39], v58 offset:3072
	ds_read_b128 v[66:69], v58 offset:4096
	ds_read_b128 v[70:73], v58 offset:5120
	ds_read2st64_b64 v[74:77], v59 offset0:26 offset1:28
	ds_read_b128 v[78:81], v58 offset:6144
	ds_read_b128 v[82:85], v58 offset:7168
	ds_read_b128 v[86:89], v58 offset:8192
	ds_read_b128 v[90:93], v58 offset:9216
	v_add_u32_e32 v59, s0, v65
	ds_read_b128 v[94:97], v58 offset:10240
	ds_read_b128 v[98:101], v59
	s_waitcnt lgkmcnt(0)
	s_nop 0
	s_nop 0
	s_nop 0
	s_nop 0
	s_waitcnt lgkmcnt(0)
	v_lshlrev_b32_e32 v110, 16, v26
	v_and_b32_e32 v111, 0xffff0000, v26
	v_lshlrev_b32_e32 v112, 16, v27
	v_and_b32_e32 v113, 0xffff0000, v27
	s_nop 1
	v_mfma_f32_16x16x32_bf16 v[2:5], v[18:21], v[102:105], v[110:113]
	v_lshlrev_b32_e32 v26, 16, v28
	v_and_b32_e32 v27, 0xffff0000, v28
	v_lshlrev_b32_e32 v28, 16, v29
	v_mfma_f32_16x16x32_bf16 v[86:89], v[102:105], v[86:89], 0
	v_and_b32_e32 v29, 0xffff0000, v29
	s_mov_b64 s[0:1], -1
	s_cmp_gt_u32 s46, 15
	v_mfma_f32_16x16x32_bf16 v[2:5], v[22:25], v[106:109], v[2:5]
	v_mfma_f32_16x16x32_bf16 v[6:9], v[30:33], v[102:105], v[26:29]
	v_lshlrev_b32_e32 v30, 16, v76
	v_and_b32_e32 v31, 0xffff0000, v76
	v_lshlrev_b32_e32 v32, 16, v77
	v_lshlrev_b32_e32 v26, 16, v74
	v_and_b32_e32 v27, 0xffff0000, v74
	v_lshlrev_b32_e32 v28, 16, v75
	v_and_b32_e32 v29, 0xffff0000, v75
	v_and_b32_e32 v33, 0xffff0000, v77
	v_mfma_f32_16x16x32_bf16 v[86:89], v[106:109], v[90:93], v[86:89]
	v_mfma_f32_16x16x32_bf16 v[10:13], v[66:69], v[102:105], v[26:29]
	v_mfma_f32_16x16x32_bf16 v[14:17], v[78:81], v[102:105], v[30:33]
	v_mfma_f32_16x16x32_bf16 v[6:9], v[36:39], v[106:109], v[6:9]
	v_mfma_f32_16x16x32_bf16 v[10:13], v[70:73], v[106:109], v[10:13]
	v_mfma_f32_16x16x32_bf16 v[14:17], v[82:85], v[106:109], v[14:17]
	v_mfma_f32_16x16x32_bf16 v[36:39], v[98:101], v[94:97], v[86:89]
	s_cbranch_scc0 .LBB0_854
	v_readlane_b32 s0, v254, 6
	v_add_u32_e32 v58, 0xffffff00, v63
	v_readlane_b32 s1, v254, 7
	s_nop 1
	v_cndmask_b32_e64 v58, v1, v58, s[0:1]
	v_readlane_b32 s0, v254, 8
	s_nop 1
	v_add_u32_e32 v58, s0, v58
	s_mov_b64 s[0:1], 0
